# baseline (speedup 1.0000x reference)
_Z16sum_layer_kernelPKfS0_Pf:
	s_load_dwordx2 s[12:13], s[0:1], 0x8
	s_load_dwordx2 s[4:5], s[0:1], 0x0
	s_load_dwordx2 s[8:9], s[0:1], 0x10
	v_lshrrev_b32_e32 v42, 6, v0
	v_bfe_u32 v41, v0, 5, 1
	v_and_b32_e32 v40, 31, v0
	v_readfirstlane_b32 s23, v42
	v_and_b32_e32 v43, 7, v0
	v_bfe_u32 v44, v0, 3, 3
	s_lshl_b32 s3, s2, 12
	s_lshl_b32 s19, s2, 7
	s_lshl_b32 s23, s23, 12
	v_lshlrev_b32_e32 v1, 11, v41
	v_lshl_or_b32 v1, v40, 2, v1
	v_lshrrev_b32_e32 v46, 1, v44
	v_xor_b32_e32 v46, v43, v46
	v_lshlrev_b32_e32 v46, 4, v46
	v_lshl_add_u32 v35, v44, 16, v46
	v_lshl_add_u32 v35, v42, 21, v35
	v_add_u32_e32 v35, s19, v35
	v_xor_b32_e32 v86, 64, v35
	s_mov_b32 s20, 0x7fc00
	s_mov_b32 s21, 0xff800
	s_mov_b32 s22, 0x17f400
	s_mov_b32 s14, 0x200000
	s_mov_b32 s15, 0x20000
	v_and_b32_e32 v45, 63, v0
	v_lshlrev_b32_e32 v37, 4, v45
	s_add_u32 s54, s23, 0x4000
	s_mov_b32 s6, 0x800000
	s_mov_b32 s7, s15
	s_mov_b32 s10, s6
	s_mov_b32 s11, s15
	s_mov_b32 m0, s54
	s_waitcnt lgkmcnt(0)
	s_and_b32 s13, s13, 0xffff
	s_and_b32 s5, s5, 0xffff
	buffer_load_dwordx4 v37, s[12:15], s3 offen nt lds
	buffer_load_dwordx4 v37, s[12:15], s3 offen offset:1024 nt lds
	buffer_load_dwordx4 v37, s[12:15], s3 offen offset:2048 nt lds
	buffer_load_dwordx4 v37, s[12:15], s3 offen offset:3072 nt lds
	s_mov_b32 m0, s23
	s_nop 0
	buffer_load_dwordx4 v35, s[4:7], 0 offen nt lds
	buffer_load_dwordx4 v86, s[4:7], s20 offen offset:1024 nt lds
	buffer_load_dwordx4 v35, s[4:7], s21 offen offset:2048 nt lds
	buffer_load_dwordx4 v86, s[4:7], s22 offen offset:3072 nt lds
	v_lshlrev_b32_e32 v36, 2, v40
	v_lshl_add_u32 v36, v41, 18, v36
	v_lshl_add_u32 v36, v42, 21, v36
	v_add_u32_e32 v36, s19, v36
	v_bfe_u32 v47, v40, 1, 3
	v_lshlrev_b32_e32 v39, 2, v41
	v_xor_b32_e32 v39, v39, v47
	v_lshlrev_b32_e32 v39, 4, v39
	v_lshl_add_u32 v39, v40, 7, v39
	v_lshl_add_u32 v39, v42, 12, v39
	v_xor_b32_e32 v81, 16, v39
	v_xor_b32_e32 v82, 32, v39
	v_xor_b32_e32 v83, 48, v39
	v_cmp_gt_u32_e32 vcc, 32, v45
	v_mov_b32_e32 v34, 0xc1600000
	v_mov_b32_e32 v84, 0x3fb8aa3b
	v_mov_b32_e32 v85, 0x3f317218
	s_lshl_b32 s36, 25, 16
	s_lshl_b32 s37, 26, 16
	s_lshl_b32 s38, 27, 16
	s_and_b32 s9, s9, 0xffff
	v_lshl_add_u32 v38, v42, 12, v1
	v_add_u32_e32 v38, 0x4000, v38
	v_add_u32_e32 v87, 0x400, v38
	s_waitcnt vmcnt(4)
	ds_read2_b32 v[18:19], v38 offset0:0 offset1:32
	ds_read2_b32 v[20:21], v38 offset0:64 offset1:96
	ds_read2_b32 v[22:23], v38 offset0:128 offset1:160
	ds_read2_b32 v[24:25], v38 offset0:192 offset1:224
	ds_read2_b32 v[26:27], v87 offset0:0 offset1:32
	ds_read2_b32 v[28:29], v87 offset0:64 offset1:96
	ds_read2_b32 v[30:31], v87 offset0:128 offset1:160
	ds_read2_b32 v[32:33], v87 offset0:192 offset1:224
	s_waitcnt lgkmcnt(0)
	v_max3_f32 v48, v18, v19, v20
	v_max3_f32 v50, v21, v22, v23
	v_max3_f32 v48, v48, v24, v25
	v_max3_f32 v50, v50, v26, v27
	v_max3_f32 v48, v48, v28, v29
	v_max3_f32 v50, v50, v30, v31
	v_max3_f32 v48, v48, v32, v33
	v_max_f32_e32 v48, v48, v50
	v_mov_b32_e32 v50, v48
	s_nop 1
	v_permlane32_swap_b32_e32 v48, v50
	v_max_f32_e32 v48, v48, v50
	v_fmamk_f32 v48, v48, 0x3fb8aa3b, v34
	v_pk_fma_f32 v[18:19], v[18:19], v[84:85], v[48:49] op_sel_hi:[1,0,0] neg_lo:[0,0,1] neg_hi:[0,0,1]
	v_exp_f32_e32 v18, v18
	v_exp_f32_e32 v19, v19
	v_pk_fma_f32 v[20:21], v[20:21], v[84:85], v[48:49] op_sel_hi:[1,0,0] neg_lo:[0,0,1] neg_hi:[0,0,1]
	v_exp_f32_e32 v20, v20
	v_exp_f32_e32 v21, v21
	v_pk_fma_f32 v[22:23], v[22:23], v[84:85], v[48:49] op_sel_hi:[1,0,0] neg_lo:[0,0,1] neg_hi:[0,0,1]
	v_exp_f32_e32 v22, v22
	v_exp_f32_e32 v23, v23
	v_pk_fma_f32 v[24:25], v[24:25], v[84:85], v[48:49] op_sel_hi:[1,0,0] neg_lo:[0,0,1] neg_hi:[0,0,1]
	v_exp_f32_e32 v24, v24
	v_exp_f32_e32 v25, v25
	v_pk_fma_f32 v[26:27], v[26:27], v[84:85], v[48:49] op_sel_hi:[1,0,0] neg_lo:[0,0,1] neg_hi:[0,0,1]
	v_exp_f32_e32 v26, v26
	v_exp_f32_e32 v27, v27
	v_pk_fma_f32 v[28:29], v[28:29], v[84:85], v[48:49] op_sel_hi:[1,0,0] neg_lo:[0,0,1] neg_hi:[0,0,1]
	v_exp_f32_e32 v28, v28
	v_exp_f32_e32 v29, v29
	v_pk_fma_f32 v[30:31], v[30:31], v[84:85], v[48:49] op_sel_hi:[1,0,0] neg_lo:[0,0,1] neg_hi:[0,0,1]
	v_exp_f32_e32 v30, v30
	v_exp_f32_e32 v31, v31
	v_pk_fma_f32 v[32:33], v[32:33], v[84:85], v[48:49] op_sel_hi:[1,0,0] neg_lo:[0,0,1] neg_hi:[0,0,1]
	v_exp_f32_e32 v32, v32
	v_exp_f32_e32 v33, v33
	v_pk_add_f32 v[56:57], v[18:19], v[20:21]
	v_pk_add_f32 v[58:59], v[22:23], v[24:25]
	v_pk_add_f32 v[60:61], v[26:27], v[28:29]
	v_pk_add_f32 v[62:63], v[30:31], v[32:33]
	v_pk_add_f32 v[56:57], v[56:57], v[58:59]
	v_pk_add_f32 v[60:61], v[60:61], v[62:63]
	v_pk_add_f32 v[56:57], v[56:57], v[60:61]
	v_add_f32_e32 v50, v56, v57
	v_mov_b32_e32 v51, v50
	s_nop 1
	v_permlane32_swap_b32_e32 v50, v51
	v_add_f32_e32 v50, v50, v51
	v_log_f32_e32 v50, v50
	v_cvt_pk_f16_f32 v40, v18, v19
	v_cvt_pk_f16_f32 v41, v20, v21
	v_cvt_pk_f16_f32 v42, v22, v23
	v_cvt_pk_f16_f32 v43, v24, v25
	v_cvt_pk_f16_f32 v44, v26, v27
	v_cvt_pk_f16_f32 v45, v28, v29
	v_cvt_pk_f16_f32 v46, v30, v31
	v_cvt_pk_f16_f32 v47, v32, v33
	v_add_f32_e32 v50, 0x41600000, v50
	v_mul_f32_e32 v50, 0xbf317218, v50
	v_cndmask_b32_e64 v51, v50, 1.0, vcc
	s_waitcnt vmcnt(0)
	ds_read_b128 v[2:5], v39
	ds_read_b128 v[6:9], v81
	ds_read_b128 v[10:13], v82
	ds_read_b128 v[14:17], v83
	s_waitcnt lgkmcnt(2)
	v_max3_f32 v52, v2, v3, v4
	v_max3_f32 v53, v5, v6, v7
	v_max_f32_e32 v52, v52, v8
	v_max_f32_e32 v53, v53, v9
	s_waitcnt lgkmcnt(0)
	v_max3_f32 v52, v52, v10, v11
	v_max3_f32 v53, v53, v12, v13
	v_max3_f32 v52, v52, v14, v15
	v_max3_f32 v53, v53, v16, v17
	v_max_f32_e32 v52, v52, v53
	v_mov_b32_e32 v53, v52
	s_nop 1
	v_permlane32_swap_b32_e32 v52, v53
	v_max_f32_e32 v52, v52, v53
	v_cndmask_b32_e32 v54, 1.0, v52, vcc
	v_fmamk_f32 v48, v52, 0x3fb8aa3b, v34
	v_pk_fma_f32 v[2:3], v[2:3], v[84:85], v[48:49] op_sel_hi:[1,0,0] neg_lo:[0,0,1] neg_hi:[0,0,1]
	v_mfma_f32_32x32x2_f32 v[64:79], v54, v51, 0
	v_exp_f32_e32 v2, v2
	v_exp_f32_e32 v3, v3
	v_pk_fma_f32 v[4:5], v[4:5], v[84:85], v[48:49] op_sel_hi:[1,0,0] neg_lo:[0,0,1] neg_hi:[0,0,1]
	v_exp_f32_e32 v4, v4
	v_exp_f32_e32 v5, v5
	v_pk_fma_f32 v[6:7], v[6:7], v[84:85], v[48:49] op_sel_hi:[1,0,0] neg_lo:[0,0,1] neg_hi:[0,0,1]
	v_exp_f32_e32 v6, v6
	v_exp_f32_e32 v7, v7
	v_pk_fma_f32 v[8:9], v[8:9], v[84:85], v[48:49] op_sel_hi:[1,0,0] neg_lo:[0,0,1] neg_hi:[0,0,1]
	v_exp_f32_e32 v8, v8
	v_exp_f32_e32 v9, v9
	v_pk_fma_f32 v[10:11], v[10:11], v[84:85], v[48:49] op_sel_hi:[1,0,0] neg_lo:[0,0,1] neg_hi:[0,0,1]
	v_exp_f32_e32 v10, v10
	v_cvt_pk_f16_f32 v56, v2, v3
	v_cvt_pk_f16_f32 v57, v4, v5
	v_cvt_pk_f16_f32 v58, v6, v7
	v_cvt_pk_f16_f32 v59, v8, v9
	v_exp_f32_e32 v11, v11
	v_pk_fma_f32 v[12:13], v[12:13], v[84:85], v[48:49] op_sel_hi:[1,0,0] neg_lo:[0,0,1] neg_hi:[0,0,1]
	v_exp_f32_e32 v12, v12
	v_mfma_f32_32x32x16_f16 v[18:33], v[56:59], v[40:43], 0
	v_exp_f32_e32 v13, v13
	v_pk_fma_f32 v[14:15], v[14:15], v[84:85], v[48:49] op_sel_hi:[1,0,0] neg_lo:[0,0,1] neg_hi:[0,0,1]
	v_exp_f32_e32 v14, v14
	v_exp_f32_e32 v15, v15
	v_pk_fma_f32 v[16:17], v[16:17], v[84:85], v[48:49] op_sel_hi:[1,0,0] neg_lo:[0,0,1] neg_hi:[0,0,1]
	v_exp_f32_e32 v16, v16
	v_exp_f32_e32 v17, v17
	v_cvt_pk_f16_f32 v60, v10, v11
	v_cvt_pk_f16_f32 v61, v12, v13
	v_cvt_pk_f16_f32 v62, v14, v15
	v_cvt_pk_f16_f32 v63, v16, v17
	s_nop 1
	v_mfma_f32_32x32x16_f16 v[18:33], v[60:63], v[44:47], v[18:33]
	s_lshl_b32 s24, 1, 16
	s_lshl_b32 s25, 2, 16
	s_lshl_b32 s26, 3, 16
	s_lshl_b32 s27, 8, 16
	s_lshl_b32 s28, 9, 16
	s_lshl_b32 s29, 10, 16
	s_lshl_b32 s30, 11, 16
	s_lshl_b32 s31, 16, 16
	s_lshl_b32 s32, 17, 16
	s_lshl_b32 s33, 18, 16
	s_lshl_b32 s34, 19, 16
	s_lshl_b32 s35, 24, 16
	v_log_f32_e32 v18, v18
	v_log_f32_e32 v19, v19
	v_log_f32_e32 v20, v20
	v_log_f32_e32 v21, v21
	v_log_f32_e32 v22, v22
	v_log_f32_e32 v23, v23
	v_pk_fma_f32 v[64:65], v[18:19], v[84:85], v[64:65] op_sel:[0,1,0] op_sel_hi:[1,1,1]
	buffer_store_dword v64, v36, s[8:11], 0 offen
	buffer_store_dword v65, v36, s[8:11], s24 offen
	v_log_f32_e32 v24, v24
	v_log_f32_e32 v25, v25
	v_pk_fma_f32 v[66:67], v[20:21], v[84:85], v[66:67] op_sel:[0,1,0] op_sel_hi:[1,1,1]
	buffer_store_dword v66, v36, s[8:11], s25 offen
	buffer_store_dword v67, v36, s[8:11], s26 offen
	v_log_f32_e32 v26, v26
	v_log_f32_e32 v27, v27
	v_pk_fma_f32 v[68:69], v[22:23], v[84:85], v[68:69] op_sel:[0,1,0] op_sel_hi:[1,1,1]
	buffer_store_dword v68, v36, s[8:11], s27 offen
	buffer_store_dword v69, v36, s[8:11], s28 offen
	v_log_f32_e32 v28, v28
	v_log_f32_e32 v29, v29
	v_pk_fma_f32 v[70:71], v[24:25], v[84:85], v[70:71] op_sel:[0,1,0] op_sel_hi:[1,1,1]
	buffer_store_dword v70, v36, s[8:11], s29 offen
	buffer_store_dword v71, v36, s[8:11], s30 offen
	v_log_f32_e32 v30, v30
	v_log_f32_e32 v31, v31
	v_pk_fma_f32 v[72:73], v[26:27], v[84:85], v[72:73] op_sel:[0,1,0] op_sel_hi:[1,1,1]
	buffer_store_dword v72, v36, s[8:11], s31 offen
	buffer_store_dword v73, v36, s[8:11], s32 offen
	v_log_f32_e32 v32, v32
	v_log_f32_e32 v33, v33
	v_pk_fma_f32 v[74:75], v[28:29], v[84:85], v[74:75] op_sel:[0,1,0] op_sel_hi:[1,1,1]
	buffer_store_dword v74, v36, s[8:11], s33 offen
	buffer_store_dword v75, v36, s[8:11], s34 offen
	v_pk_fma_f32 v[76:77], v[30:31], v[84:85], v[76:77] op_sel:[0,1,0] op_sel_hi:[1,1,1]
	buffer_store_dword v76, v36, s[8:11], s35 offen
	buffer_store_dword v77, v36, s[8:11], s36 offen
	v_pk_fma_f32 v[78:79], v[32:33], v[84:85], v[78:79] op_sel:[0,1,0] op_sel_hi:[1,1,1]
	buffer_store_dword v78, v36, s[8:11], s37 offen
	buffer_store_dword v79, v36, s[8:11], s38 offen
	s_endpgm
